# speedup vs baseline: 1.0181x; 1.0165x over previous
_Z6k_gramILi0EEvPK15HIP_vector_typeIjLj4EEPyPf:
	s_load_dwordx4 s[8:11], s[0:1], 0x0
	s_load_dwordx2 s[4:5], s[0:1], 0x10
	s_lshl_b32 s0, s2, 2
	s_and_b32 s0, s0, 28
	s_ashr_i32 s1, s2, 6
	s_add_i32 s16, s0, s1
	v_readfirstlane_b32 s23, v0
	s_ashr_i32 s17, s16, 31
	s_lshr_b32 s21, s23, 6
	s_bfe_u32 s18, s23, 0x20006
	s_lshr_b32 s22, s2, 3
	s_bfe_u32 s20, s2, 0x30003
	s_lshl_b64 s[0:1], s[16:17], 20
	s_waitcnt lgkmcnt(0)
	s_add_u32 s12, s8, s0
	v_mov_b32_e32 v1, 0x20000
	s_addc_u32 s0, s9, s1
	s_lshl_b32 s1, s20, 2
	v_lshl_or_b32 v1, v0, 2, v1
	v_bfrev_b32_e32 v2, 1
	s_cmp_lt_u32 s20, 4
	ds_write_b32 v1, v2
	s_mov_b32 s24, 4
	s_mov_b32 s15, 0x20000
	s_and_b32 s13, s0, 0xffff
	s_mov_b32 s14, 0x100000
	v_lshlrev_b32_e32 v166, 4, v0
	s_lshl_b32 s25, s21, 10
	s_lshl_b32 s0, s20, 17
	s_mov_b32 m0, s25
	s_nop 0
	buffer_load_dwordx4 v166, s[12:15], s0 offen lds
	s_add_i32 s27, s25, 0x4000
	s_or_b32 s2, s0, 0x8000
	s_mov_b32 m0, s27
	s_nop 0
	buffer_load_dwordx4 v166, s[12:15], s2 offen lds
	s_add_i32 s34, s25, 0x10000
	s_or_b32 s2, s0, 0x10000
	s_mov_b32 m0, s34
	s_nop 0
	buffer_load_dwordx4 v166, s[12:15], s2 offen lds
	s_add_i32 s36, s25, 0x14000
	s_or_b32 s2, s0, 0x18000
	s_mov_b32 m0, s36
	s_nop 0
	buffer_load_dwordx4 v166, s[12:15], s2 offen lds
	s_add_i32 s26, s25, 0x2000
	s_or_b32 s2, s0, 0x2000
	s_mov_b32 m0, s26
	s_nop 0
	buffer_load_dwordx4 v166, s[12:15], s2 offen lds
	s_add_i32 s28, s25, 0x6000
	s_or_b32 s2, s0, 0xa000
	s_mov_b32 m0, s28
	s_nop 0
	buffer_load_dwordx4 v166, s[12:15], s2 offen lds
	s_add_i32 s35, s25, 0x12000
	s_or_b32 s2, s0, 0x12000
	s_mov_b32 m0, s35
	s_nop 0
	buffer_load_dwordx4 v166, s[12:15], s2 offen lds
	s_add_i32 s37, s25, 0x16000
	s_or_b32 s2, s0, 0x1a000
	s_mov_b32 m0, s37
	s_nop 0
	buffer_load_dwordx4 v166, s[12:15], s2 offen lds
	s_add_i32 s29, s25, 0x8000
	s_or_b32 s2, s0, 0x4000
	s_mov_b32 m0, s29
	s_nop 0
	buffer_load_dwordx4 v166, s[12:15], s2 offen lds
	s_add_i32 s30, s25, 0xa000
	s_or_b32 s2, s0, 0x6000
	s_mov_b32 m0, s30
	s_nop 0
	buffer_load_dwordx4 v166, s[12:15], s2 offen lds
	s_add_i32 s31, s25, 0xc000
	s_or_b32 s2, s0, 0xc000
	s_mov_b32 m0, s31
	s_nop 0
	buffer_load_dwordx4 v166, s[12:15], s2 offen lds
	s_add_i32 s33, s25, 0xe000
	s_or_b32 s2, s0, 0xe000
	s_mov_b32 m0, s33
	s_nop 0
	buffer_load_dwordx4 v166, s[12:15], s2 offen lds
	s_add_i32 s38, s25, 0x18000
	s_or_b32 s2, s0, 0x14000
	s_mov_b32 m0, s38
	s_nop 0
	buffer_load_dwordx4 v166, s[12:15], s2 offen lds
	s_add_i32 s39, s25, 0x1a000
	s_or_b32 s2, s0, 0x16000
	s_mov_b32 m0, s39
	s_nop 0
	buffer_load_dwordx4 v166, s[12:15], s2 offen lds
	s_add_i32 s40, s25, 0x1c000
	s_or_b32 s2, s0, 0x1c000
	s_mov_b32 m0, s40
	s_nop 0
	buffer_load_dwordx4 v166, s[12:15], s2 offen lds
	s_add_i32 s42, s25, 0x1e000
	s_or_b32 s2, s0, 0x1e000
	s_mov_b32 m0, s42
	s_nop 0
	buffer_load_dwordx4 v166, s[12:15], s2 offen lds
	s_lshl_b32 s0, s23, 9
	s_lshl_b32 s2, s23, 8
	v_and_b32_e32 v167, 15, v0
	v_bfe_u32 v160, v0, 4, 2
	s_and_b32 s0, s0, 0x10000
	s_and_b32 s2, s2, 0x4000
	v_lshlrev_b32_e32 v128, 9, v160
	v_lshlrev_b32_e32 v129, 4, v167
	s_or_b32 s0, s0, s2
	v_or3_b32 v124, s0, v128, v129
	s_waitcnt vmcnt(12)
	s_waitcnt lgkmcnt(0)
	s_barrier
	s_lshr_b32 s41, s23, 8
	s_lshl_b32 s0, s41, 14
	s_lshl_b32 s50, s24, 2
	v_or3_b32 v168, s0, v128, v129
	s_or_b32 s43, s18, s1
	s_lshl_b32 s0, s16, 10
	s_lshl_b32 s1, s43, 5
	ds_read_b128 v[128:131], v168
	ds_read_b128 v[132:135], v168 offset:256
	ds_read_b128 v[136:139], v168 offset:2048
	ds_read_b128 v[140:143], v168 offset:2304
	s_or_b32 s0, s1, s0
	v_or_b32_e32 v144, s0, v167
	v_lshlrev_b32_e32 v146, 2, v160
	v_ashrrev_i32_e32 v145, 31, v144
	v_lshl_add_u64 v[164:165], v[144:145], 2, s[4:5]
	v_or_b32_e32 v144, 1, v146
	v_cmp_eq_u32_e64 s[2:3], v144, v167
	v_or_b32_e32 v144, 2, v146
	v_cmp_eq_u32_e64 s[4:5], v144, v167
	v_or_b32_e32 v144, 3, v146
	s_add_i32 s44, s50, 3
	s_lshl_b32 s45, s22, 2
	v_cmp_eq_u32_e64 s[0:1], v146, v167
	v_cmp_eq_u32_e64 s[6:7], v144, v167
	v_add_u32_e32 v169, 0x10000, v168
	v_add_u32_e32 v170, 0x10100, v168
	v_add_u32_e32 v171, 0x10800, v168
	v_add_u32_e32 v172, 0x10900, v168
	s_and_b32 s8, s45, 28
	s_add_i32 s8, s8, s41
	s_lshl_b32 s19, s8, 1
	s_or_b32 s51, s19, 1
	v_mov_b32_e32 v234, s19
	v_mov_b32_e32 v235, s51
	s_and_b32 s46, s21, 3
	s_lshl_b32 s46, s46, 5
	v_lshl_or_b32 v173, v160, 3, s46
	s_lshl_b32 s47, s41, 7
	s_mov_b32 s48, 0
	s_movk_i32 s49, 0xffc0
	v_add_u32_e32 v174, 0x11000, v168
	v_add_u32_e32 v175, 0x11100, v168
	v_add_u32_e32 v176, 0x11800, v168
	v_add_u32_e32 v177, 0x11900, v168
	v_add_u32_e32 v178, 0x12000, v168
	v_add_u32_e32 v179, 0x12100, v168
	v_add_u32_e32 v180, 0x12800, v168
	v_add_u32_e32 v181, 0x12900, v168
	v_add_u32_e32 v182, 0x13000, v168
	v_add_u32_e32 v183, 0x13100, v168
	v_add_u32_e32 v184, 0x13800, v168
	v_add_u32_e32 v185, 0x13900, v168
	v_add_u32_e32 v186, 0x18000, v168
	v_add_u32_e32 v187, 0x18100, v168
	v_add_u32_e32 v188, 0x18800, v168
	v_add_u32_e32 v189, 0x18900, v168
	v_add_u32_e32 v190, 0x19000, v168
	v_add_u32_e32 v191, 0x19100, v168
	v_add_u32_e32 v192, 0x19800, v168
	v_add_u32_e32 v193, 0x19900, v168
	v_add_u32_e32 v194, 0x1a000, v168
	v_add_u32_e32 v195, 0x1a100, v168
	v_add_u32_e32 v196, 0x1a800, v168
	v_add_u32_e32 v197, 0x1a900, v168
	v_add_u32_e32 v198, 0x1b000, v168
	v_add_u32_e32 v199, 0x1b100, v168
	v_add_u32_e32 v200, 0x1b800, v168
	v_add_u32_e32 v201, 0x1b900, v168
	ds_read_b128 v[0:3], v124
	ds_read_b128 v[4:7], v124 offset:256
	ds_read_b128 v[8:11], v124 offset:2048
	ds_read_b128 v[12:15], v124 offset:2304
	ds_read_b128 v[144:147], v168
	ds_read_b128 v[148:151], v168 offset:256
	ds_read_b128 v[152:155], v168 offset:2048
	ds_read_b128 v[156:159], v168 offset:2304
	ds_read_b128 v[224:227], v168 offset:4096
	s_waitcnt lgkmcnt(4)
	v_mfma_f32_16x16x32_bf16 v[208:211], v[0:3], v[144:147], 0
	v_mfma_f32_16x16x32_bf16 v[212:215], v[4:7], v[144:147], 0
	ds_read_b128 v[228:231], v168 offset:4352
	ds_read_b128 v[16:19], v124 offset:4096
	ds_read_b128 v[20:23], v124 offset:4352
	s_waitcnt lgkmcnt(6)
	v_mfma_f32_16x16x32_bf16 v[216:219], v[0:3], v[148:151], 0
	v_mfma_f32_16x16x32_bf16 v[220:223], v[4:7], v[148:151], 0
	ds_read_b128 v[144:147], v168 offset:6144
	s_waitcnt lgkmcnt(6)
	v_mfma_f32_16x16x32_bf16 v[208:211], v[8:11], v[152:155], v[208:211]
	v_mfma_f32_16x16x32_bf16 v[212:215], v[12:15], v[152:155], v[212:215]
	ds_read_b128 v[148:151], v168 offset:6400
	ds_read_b128 v[24:27], v124 offset:6144
	ds_read_b128 v[28:31], v124 offset:6400
	s_waitcnt lgkmcnt(8)
	v_mfma_f32_16x16x32_bf16 v[216:219], v[8:11], v[156:159], v[216:219]
	v_mfma_f32_16x16x32_bf16 v[220:223], v[12:15], v[156:159], v[220:223]
	s_waitcnt lgkmcnt(4)
	v_mfma_f32_16x16x32_bf16 v[208:211], v[16:19], v[224:227], v[208:211]
	v_mfma_f32_16x16x32_bf16 v[212:215], v[20:23], v[224:227], v[212:215]
	v_mfma_f32_16x16x32_bf16 v[216:219], v[16:19], v[228:231], v[216:219]
	v_mfma_f32_16x16x32_bf16 v[220:223], v[20:23], v[228:231], v[220:223]
	s_waitcnt lgkmcnt(0)
	v_mfma_f32_16x16x32_bf16 v[208:211], v[24:27], v[144:147], v[208:211]
	v_mfma_f32_16x16x32_bf16 v[212:215], v[28:31], v[144:147], v[212:215]
	v_mfma_f32_16x16x32_bf16 v[216:219], v[24:27], v[148:151], v[216:219]
	v_mfma_f32_16x16x32_bf16 v[220:223], v[28:31], v[148:151], v[220:223]
	s_waitcnt vmcnt(8)
	s_barrier
	ds_read_b128 v[152:155], v168 offset:8192
	ds_read_b128 v[156:159], v168 offset:8448
	ds_read_b128 v[224:227], v168 offset:10240
	ds_read_b128 v[228:231], v168 offset:10496
	ds_read_b128 v[144:147], v168 offset:12288
	ds_read_b128 v[32:35], v124 offset:8192
	ds_read_b128 v[36:39], v124 offset:8448
	ds_read_b128 v[40:43], v124 offset:10240
	ds_read_b128 v[44:47], v124 offset:10496
	s_waitcnt lgkmcnt(2)
	v_mfma_f32_16x16x32_bf16 v[208:211], v[32:35], v[152:155], v[208:211]
	v_mfma_f32_16x16x32_bf16 v[212:215], v[36:39], v[152:155], v[212:215]
	ds_read_b128 v[148:151], v168 offset:12544
	ds_read_b128 v[48:51], v124 offset:12288
	ds_read_b128 v[52:55], v124 offset:12544
	v_mfma_f32_16x16x32_bf16 v[216:219], v[32:35], v[156:159], v[216:219]
	v_mfma_f32_16x16x32_bf16 v[220:223], v[36:39], v[156:159], v[220:223]
	ds_read_b128 v[152:155], v168 offset:14336
	s_waitcnt lgkmcnt(4)
	v_mfma_f32_16x16x32_bf16 v[208:211], v[40:43], v[224:227], v[208:211]
	v_mfma_f32_16x16x32_bf16 v[212:215], v[44:47], v[224:227], v[212:215]
	ds_read_b128 v[156:159], v168 offset:14592
	ds_read_b128 v[56:59], v124 offset:14336
	ds_read_b128 v[60:63], v124 offset:14592
	v_mfma_f32_16x16x32_bf16 v[216:219], v[40:43], v[228:231], v[216:219]
	v_mfma_f32_16x16x32_bf16 v[220:223], v[44:47], v[228:231], v[220:223]
	s_waitcnt lgkmcnt(4)
	v_mfma_f32_16x16x32_bf16 v[208:211], v[48:51], v[144:147], v[208:211]
	v_mfma_f32_16x16x32_bf16 v[212:215], v[52:55], v[144:147], v[212:215]
	v_mfma_f32_16x16x32_bf16 v[216:219], v[48:51], v[148:151], v[216:219]
	v_mfma_f32_16x16x32_bf16 v[220:223], v[52:55], v[148:151], v[220:223]
	s_waitcnt lgkmcnt(0)
	v_mfma_f32_16x16x32_bf16 v[208:211], v[56:59], v[152:155], v[208:211]
	v_mfma_f32_16x16x32_bf16 v[212:215], v[60:63], v[152:155], v[212:215]
	v_mfma_f32_16x16x32_bf16 v[216:219], v[56:59], v[156:159], v[216:219]
	v_mfma_f32_16x16x32_bf16 v[220:223], v[60:63], v[156:159], v[220:223]
	s_barrier
	s_add_i32 s60, s45, 4
	s_and_b32 s60, s60, 28
	s_lshl_b32 s60, s60, 15
	ds_read_b128 v[144:147], v169
	ds_read_b128 v[148:151], v169 offset:256
	ds_read_b128 v[152:155], v169 offset:2048
	ds_read_b128 v[156:159], v169 offset:2304
	ds_read_b128 v[224:227], v169 offset:4096
	s_waitcnt lgkmcnt(4)
	v_mfma_f32_16x16x32_bf16 v[136:139], v[0:3], v[144:147], 0
	v_mfma_f32_16x16x32_bf16 v[128:131], v[4:7], v[144:147], 0
	ds_read_b128 v[228:231], v169 offset:4352
	s_waitcnt lgkmcnt(4)
	v_mfma_f32_16x16x32_bf16 v[140:143], v[0:3], v[148:151], 0
	v_mfma_f32_16x16x32_bf16 v[132:135], v[4:7], v[148:151], 0
	ds_read_b128 v[144:147], v169 offset:6144
	s_waitcnt lgkmcnt(4)
	v_mfma_f32_16x16x32_bf16 v[136:139], v[8:11], v[152:155], v[136:139]
	v_mfma_f32_16x16x32_bf16 v[128:131], v[12:15], v[152:155], v[128:131]
	ds_read_b128 v[148:151], v169 offset:6400
	s_waitcnt lgkmcnt(4)
	v_mfma_f32_16x16x32_bf16 v[140:143], v[8:11], v[156:159], v[140:143]
	v_mfma_f32_16x16x32_bf16 v[132:135], v[12:15], v[156:159], v[132:135]
	ds_read_b128 v[152:155], v169 offset:8192
	s_waitcnt lgkmcnt(4)
	v_mfma_f32_16x16x32_bf16 v[136:139], v[16:19], v[224:227], v[136:139]
	v_mfma_f32_16x16x32_bf16 v[128:131], v[20:23], v[224:227], v[128:131]
	ds_read_b128 v[156:159], v169 offset:8448
	s_waitcnt lgkmcnt(4)
	v_mfma_f32_16x16x32_bf16 v[140:143], v[16:19], v[228:231], v[140:143]
	v_mfma_f32_16x16x32_bf16 v[132:135], v[20:23], v[228:231], v[132:135]
	ds_read_b128 v[224:227], v169 offset:10240
	s_waitcnt lgkmcnt(4)
	v_mfma_f32_16x16x32_bf16 v[136:139], v[24:27], v[144:147], v[136:139]
	v_mfma_f32_16x16x32_bf16 v[128:131], v[28:31], v[144:147], v[128:131]
	ds_read_b128 v[228:231], v169 offset:10496
	s_waitcnt lgkmcnt(4)
	v_mfma_f32_16x16x32_bf16 v[140:143], v[24:27], v[148:151], v[140:143]
	v_mfma_f32_16x16x32_bf16 v[132:135], v[28:31], v[148:151], v[132:135]
	ds_read_b128 v[144:147], v169 offset:12288
	s_waitcnt vmcnt(0)
	s_barrier
	s_waitcnt lgkmcnt(4)
	v_mfma_f32_16x16x32_bf16 v[136:139], v[32:35], v[152:155], v[136:139]
	v_mfma_f32_16x16x32_bf16 v[128:131], v[36:39], v[152:155], v[128:131]
	ds_read_b128 v[148:151], v169 offset:12544
	ds_read_b128 v[64:67], v124 offset:32768
	ds_read_b128 v[68:71], v124 offset:33024
	s_waitcnt lgkmcnt(6)
	v_mfma_f32_16x16x32_bf16 v[140:143], v[32:35], v[156:159], v[140:143]
	s_mov_b32 s61, s60
	s_mov_b32 m0, s25
	s_nop 0
	buffer_load_dwordx4 v166, s[12:15], s61 offen lds
	v_mfma_f32_16x16x32_bf16 v[132:135], v[36:39], v[156:159], v[132:135]
	ds_read_b128 v[152:155], v169 offset:14336
	ds_read_b128 v[72:75], v124 offset:34816
	ds_read_b128 v[76:79], v124 offset:35072
	s_waitcnt lgkmcnt(8)
	v_mfma_f32_16x16x32_bf16 v[136:139], v[40:43], v[224:227], v[136:139]
	v_mfma_f32_16x16x32_bf16 v[128:131], v[44:47], v[224:227], v[128:131]
	ds_read_b128 v[156:159], v169 offset:14592
	ds_read_b128 v[80:83], v124 offset:36864
	ds_read_b128 v[84:87], v124 offset:37120
	s_waitcnt lgkmcnt(10)
	v_mfma_f32_16x16x32_bf16 v[140:143], v[40:43], v[228:231], v[140:143]
	s_or_b32 s61, s60, 0x2000
	s_mov_b32 m0, s26
	s_nop 0
	buffer_load_dwordx4 v166, s[12:15], s61 offen lds
	v_mfma_f32_16x16x32_bf16 v[132:135], v[44:47], v[228:231], v[132:135]
	ds_read_b128 v[88:91], v124 offset:38912
	ds_read_b128 v[92:95], v124 offset:39168
	s_waitcnt lgkmcnt(11)
	v_mfma_f32_16x16x32_bf16 v[136:139], v[48:51], v[144:147], v[136:139]
	v_mfma_f32_16x16x32_bf16 v[128:131], v[52:55], v[144:147], v[128:131]
	ds_read_b128 v[96:99], v124 offset:40960
	ds_read_b128 v[100:103], v124 offset:41216
	s_waitcnt lgkmcnt(12)
	v_mfma_f32_16x16x32_bf16 v[140:143], v[48:51], v[148:151], v[140:143]
	s_or_b32 s61, s60, 0x8000
	s_mov_b32 m0, s27
	s_nop 0
	buffer_load_dwordx4 v166, s[12:15], s61 offen lds
	v_mfma_f32_16x16x32_bf16 v[132:135], v[52:55], v[148:151], v[132:135]
	ds_read_b128 v[104:107], v124 offset:43008
	ds_read_b128 v[108:111], v124 offset:43264
	s_waitcnt lgkmcnt(11)
	v_mfma_f32_16x16x32_bf16 v[136:139], v[56:59], v[152:155], v[136:139]
	v_mfma_f32_16x16x32_bf16 v[128:131], v[60:63], v[152:155], v[128:131]
	ds_read_b128 v[112:115], v124 offset:45056
	ds_read_b128 v[116:119], v124 offset:45312
	s_waitcnt lgkmcnt(10)
	v_mfma_f32_16x16x32_bf16 v[140:143], v[56:59], v[156:159], v[140:143]
	s_or_b32 s61, s60, 0xa000
	s_mov_b32 m0, s28
	s_nop 0
	buffer_load_dwordx4 v166, s[12:15], s61 offen lds
	v_mfma_f32_16x16x32_bf16 v[132:135], v[60:63], v[156:159], v[132:135]
	ds_read_b128 v[120:123], v124 offset:47104
	ds_read_b128 v[124:127], v124 offset:47360
	s_barrier
	s_add_i32 s60, s45, 4
	s_and_b32 s60, s60, 28
	s_or_b32 s60, s60, 2
	s_lshl_b32 s60, s60, 15
	ds_read_b128 v[144:147], v168 offset:32768
	ds_read_b128 v[148:151], v168 offset:33024
	ds_read_b128 v[152:155], v168 offset:34816
	ds_read_b128 v[156:159], v168 offset:35072
	ds_read_b128 v[224:227], v168 offset:36864
	s_waitcnt lgkmcnt(4)
	v_mfma_f32_16x16x32_bf16 v[208:211], v[64:67], v[144:147], v[208:211]
	v_mfma_f32_16x16x32_bf16 v[212:215], v[68:71], v[144:147], v[212:215]
	ds_read_b128 v[228:231], v168 offset:37120
	s_waitcnt lgkmcnt(4)
	v_mfma_f32_16x16x32_bf16 v[216:219], v[64:67], v[148:151], v[216:219]
	s_mov_b32 s61, s60
	s_mov_b32 m0, s34
	s_nop 0
	buffer_load_dwordx4 v166, s[12:15], s61 offen lds
	v_mfma_f32_16x16x32_bf16 v[220:223], v[68:71], v[148:151], v[220:223]
	ds_read_b128 v[144:147], v168 offset:38912
	s_waitcnt lgkmcnt(4)
	v_mfma_f32_16x16x32_bf16 v[208:211], v[72:75], v[152:155], v[208:211]
	v_mfma_f32_16x16x32_bf16 v[212:215], v[76:79], v[152:155], v[212:215]
	ds_read_b128 v[148:151], v168 offset:39168
	s_waitcnt lgkmcnt(4)
	v_mfma_f32_16x16x32_bf16 v[216:219], v[72:75], v[156:159], v[216:219]
	v_mfma_f32_16x16x32_bf16 v[220:223], v[76:79], v[156:159], v[220:223]
	ds_read_b128 v[152:155], v168 offset:40960
	s_waitcnt lgkmcnt(4)
	v_mfma_f32_16x16x32_bf16 v[208:211], v[80:83], v[224:227], v[208:211]
	v_mfma_f32_16x16x32_bf16 v[212:215], v[84:87], v[224:227], v[212:215]
	ds_read_b128 v[156:159], v168 offset:41216
	s_waitcnt lgkmcnt(4)
	v_mfma_f32_16x16x32_bf16 v[216:219], v[80:83], v[228:231], v[216:219]
	s_or_b32 s61, s60, 0x2000
	s_mov_b32 m0, s35
	s_nop 0
	buffer_load_dwordx4 v166, s[12:15], s61 offen lds
	v_mfma_f32_16x16x32_bf16 v[220:223], v[84:87], v[228:231], v[220:223]
	ds_read_b128 v[224:227], v168 offset:43008
	s_waitcnt lgkmcnt(4)
	v_mfma_f32_16x16x32_bf16 v[208:211], v[88:91], v[144:147], v[208:211]
	v_mfma_f32_16x16x32_bf16 v[212:215], v[92:95], v[144:147], v[212:215]
	ds_read_b128 v[228:231], v168 offset:43264
	s_waitcnt lgkmcnt(4)
	v_mfma_f32_16x16x32_bf16 v[216:219], v[88:91], v[148:151], v[216:219]
	v_mfma_f32_16x16x32_bf16 v[220:223], v[92:95], v[148:151], v[220:223]
	ds_read_b128 v[144:147], v168 offset:45056
	s_waitcnt lgkmcnt(4)
	v_mfma_f32_16x16x32_bf16 v[208:211], v[96:99], v[152:155], v[208:211]
	v_mfma_f32_16x16x32_bf16 v[212:215], v[100:103], v[152:155], v[212:215]
	ds_read_b128 v[148:151], v168 offset:45312
	s_waitcnt lgkmcnt(4)
	v_mfma_f32_16x16x32_bf16 v[216:219], v[96:99], v[156:159], v[216:219]
	s_or_b32 s61, s60, 0x8000
	s_mov_b32 m0, s36
	s_nop 0
	buffer_load_dwordx4 v166, s[12:15], s61 offen lds
	v_mfma_f32_16x16x32_bf16 v[220:223], v[100:103], v[156:159], v[220:223]
	ds_read_b128 v[152:155], v168 offset:47104
	s_waitcnt lgkmcnt(4)
	v_mfma_f32_16x16x32_bf16 v[208:211], v[104:107], v[224:227], v[208:211]
	v_mfma_f32_16x16x32_bf16 v[212:215], v[108:111], v[224:227], v[212:215]
	ds_read_b128 v[156:159], v168 offset:47360
	s_waitcnt lgkmcnt(4)
	v_mfma_f32_16x16x32_bf16 v[216:219], v[104:107], v[228:231], v[216:219]
	v_mfma_f32_16x16x32_bf16 v[220:223], v[108:111], v[228:231], v[220:223]
	s_waitcnt lgkmcnt(3)
	v_mfma_f32_16x16x32_bf16 v[208:211], v[112:115], v[144:147], v[208:211]
	v_mfma_f32_16x16x32_bf16 v[212:215], v[116:119], v[144:147], v[212:215]
	s_waitcnt lgkmcnt(2)
	v_mfma_f32_16x16x32_bf16 v[216:219], v[112:115], v[148:151], v[216:219]
	s_or_b32 s61, s60, 0xa000
	s_mov_b32 m0, s37
	s_nop 0
	buffer_load_dwordx4 v166, s[12:15], s61 offen lds
	v_mfma_f32_16x16x32_bf16 v[220:223], v[116:119], v[148:151], v[220:223]
	s_waitcnt lgkmcnt(1)
	v_mfma_f32_16x16x32_bf16 v[208:211], v[120:123], v[152:155], v[208:211]
	v_mfma_f32_16x16x32_bf16 v[212:215], v[124:127], v[152:155], v[212:215]
	s_waitcnt lgkmcnt(0)
	v_mfma_f32_16x16x32_bf16 v[216:219], v[120:123], v[156:159], v[216:219]
	v_mfma_f32_16x16x32_bf16 v[220:223], v[124:127], v[156:159], v[220:223]
	s_waitcnt vmcnt(4)
	s_barrier
	s_nop 7
	s_nop 3
	s_cmp_lg_u32 s8, s43
	s_cbranch_scc1 .Ldiag0_done
	s_mov_b64 s[56:57], exec
	s_and_b64 exec, s[56:57], s[0:1]
	global_store_dword v[164:165], v208, off
	v_mov_b32_e32 v208, -1.0
	global_store_dword v[164:165], v220, off offset:64
	v_mov_b32_e32 v220, -1.0
	s_and_b64 exec, s[56:57], s[2:3]
	global_store_dword v[164:165], v209, off
	v_mov_b32_e32 v209, -1.0
	global_store_dword v[164:165], v221, off offset:64
	v_mov_b32_e32 v221, -1.0
	s_and_b64 exec, s[56:57], s[4:5]
	global_store_dword v[164:165], v210, off
	v_mov_b32_e32 v210, -1.0
	global_store_dword v[164:165], v222, off offset:64
	v_mov_b32_e32 v222, -1.0
	s_and_b64 exec, s[56:57], s[6:7]
	global_store_dword v[164:165], v211, off
	v_mov_b32_e32 v211, -1.0
	global_store_dword v[164:165], v223, off offset:64
	v_mov_b32_e32 v223, -1.0
	s_mov_b64 exec, s[56:57]
